# s23 + P0: LN parameter fill loads batched (12 loads, one wait) + LN loop cross-trip prefetch of the two rows' 16 loads
# speedup vs baseline: 1.0016x; 1.0016x over previous
; #define LAS __attribute__((address_space(3)))
; #define LBAR() do { asm volatile("s_waitcnt lgkmcnt(0)" ::: "memory"); __builtin_amdgcn_s_barrier(); asm volatile("" ::: "memory"); } while (0)
; __global__ void __launch_bounds__(NTHREADS, 2) fwd(Args args) {
;     ...
;         LAS float* LGI = (LAS float*)lds; LAS float* LBI = LGI + D; LAS float* SHI = LBI + D; LAS float* SCI = SHI + 5 * D;
;         for (int i = tid; i < D / 4; i += NTHREADS) { *(LAS f32x4*)(LGI + 4 * i) = *(const f32x4*)(ln_in_g + 4 * i); *(LAS f32x4*)(LBI + 4 * i) = *(const f32x4*)(ln_in_b + 4 * i); }
;         for (int i = tid; i < 5 * D / 4; i += NTHREADS) { const int r = i / (D / 4), c = 4 * (i % (D / 4)); *(LAS f32x4*)(SHI + r * D + c) = *(const f32x4*)(MOD + r * (6 * D) + c); *(LAS f32x4*)(SCI + r * D + c) = *(const f32x4*)(MOD + r * (6 * D) + D + c); }
;         LBAR();
;         for (int m0 = gw; m0 < MR; m0 += 2 * NGW) {
;             f32x4 vv[2][8];
; #pragma unroll
;             for (int t2 = 0; t2 < 2; ++t2) { const int m = (m0 + t2 * NGW) < MR ? m0 + t2 * NGW : m0; const float* xr = m < T ? x + (size_t)m * D : ctx + (size_t)(m - T) * D;
; #pragma unroll
;                 for (int j = 0; j < 8; ++j) vv[t2][j] = *(const f32x4*)(xr + 8 * (lane + 64 * (j >> 1)) + 4 * (j & 1)); }
.LBB0_106:
	s_or_b64 exec, exec, s[0:1]
	s_barrier
	v_lshlrev_b32_e32 v1, 2, v194
	global_load_dwordx4 v[2:5], v1, s[24:25]
	global_load_dwordx4 v[6:9], v1, s[26:27]
	global_load_dwordx4 v[16:19], v1, s[96:97]
	v_add_u32_e32 v57, 0x2000, v1
	global_load_dwordx4 v[20:23], v57, s[96:97]
	v_add_u32_e32 v58, 0xc000, v1
	global_load_dwordx4 v[24:27], v58, s[96:97]
	v_add_u32_e32 v59, 0xe000, v1
	global_load_dwordx4 v[28:31], v59, s[96:97]
	v_add_u32_e32 v60, 0x18000, v1
	global_load_dwordx4 v[32:35], v60, s[96:97]
	v_add_u32_e32 v61, 0x1a000, v1
	global_load_dwordx4 v[36:39], v61, s[96:97]
	v_add_u32_e32 v62, 0x24000, v1
	global_load_dwordx4 v[40:43], v62, s[96:97]
	v_add_u32_e32 v63, 0x26000, v1
	global_load_dwordx4 v[44:47], v63, s[96:97]
	v_add_u32_e32 v64, 0x30000, v1
	global_load_dwordx4 v[48:51], v64, s[96:97]
	v_add_u32_e32 v65, 0x32000, v1
	global_load_dwordx4 v[52:55], v65, s[96:97]
	v_add_u32_e32 v10, 0x4000, v1
	v_add_u32_e32 v11, 0xe000, v1
	s_waitcnt vmcnt(0)
	ds_write_b128 v1, v[2:5]
	ds_write_b128 v1, v[6:9] offset:8192
	ds_write_b128 v10, v[16:19]
	ds_write_b128 v11, v[20:23]
	ds_write_b128 v10, v[24:27] offset:8192
	ds_write_b128 v11, v[28:31] offset:8192
	ds_write_b128 v10, v[32:35] offset:16384
	ds_write_b128 v11, v[36:39] offset:16384
	ds_write_b128 v10, v[40:43] offset:24576
	ds_write_b128 v11, v[44:47] offset:24576
	ds_write_b128 v10, v[48:51] offset:32768
	ds_write_b128 v11, v[52:55] offset:32768
	s_waitcnt lgkmcnt(0)
	s_barrier
	s_cmpk_gt_i32 s50, 0x43ff
	s_cbranch_scc1 .LBB0_124
	v_mbcnt_lo_u32_b32 v1, -1, 0
	v_mbcnt_hi_u32_b32 v2, -1, v1
	v_and_b32_e32 v1, 64, v2
	v_add_u32_e32 v3, 64, v1
	v_xor_b32_e32 v1, 1, v2
	v_cmp_lt_i32_e32 vcc, v1, v3
	v_xor_b32_e32 v4, 2, v2
	v_lshl_add_u32 v138, v220, 5, 0
	v_cndmask_b32_e32 v1, v2, v1, vcc
	v_cmp_lt_i32_e32 vcc, v4, v3
	s_mov_b32 s31, s51
	v_readlane_b32 s0, v246, 10
	v_cndmask_b32_e32 v4, v2, v4, vcc
	v_lshlrev_b32_e32 v132, 2, v4
	v_xor_b32_e32 v4, 4, v2
	v_cmp_lt_i32_e32 vcc, v4, v3
	s_ashr_i32 s51, s50, 31
	s_lshl_b32 s0, s0, 4
	v_cndmask_b32_e32 v4, v2, v4, vcc
	v_lshlrev_b32_e32 v133, 2, v4
	v_xor_b32_e32 v4, 8, v2
	v_cmp_lt_i32_e32 vcc, v4, v3
	s_lshl_b64 s[2:3], s[50:51], 12
	s_add_u32 s4, s88, s2
	v_cndmask_b32_e32 v4, v2, v4, vcc
	v_lshlrev_b32_e32 v135, 2, v4
	v_xor_b32_e32 v4, 16, v2
	v_cmp_lt_i32_e32 vcc, v4, v3
	v_readlane_b32 s1, v246, 11
	s_addc_u32 s5, s89, s3
	v_cndmask_b32_e32 v4, v2, v4, vcc
	v_lshlrev_b32_e32 v136, 2, v4
	v_xor_b32_e32 v4, 32, v2
	v_cmp_lt_i32_e32 vcc, v4, v3
	s_add_i32 s2, s50, s92
	s_ashr_i32 s1, s0, 31
	v_cndmask_b32_e32 v2, v2, v4, vcc
	v_lshlrev_b32_e32 v137, 2, v2
	ds_read_b128 v[2:5], v138
	ds_read_b128 v[6:9], v138 offset:16
	ds_read_b128 v[10:13], v138 offset:8192
	ds_read_b128 v[14:17], v138 offset:8208
	ds_read_b128 v[18:21], v138 offset:2048
	ds_read_b128 v[22:25], v138 offset:2064
	ds_read_b128 v[26:29], v138 offset:10240
	ds_read_b128 v[30:33], v138 offset:10256
	ds_read_b128 v[34:37], v138 offset:4096
	ds_read_b128 v[38:41], v138 offset:4112
	ds_read_b128 v[42:45], v138 offset:12288
	ds_read_b128 v[46:49], v138 offset:12304
	ds_read_b128 v[50:53], v138 offset:6144
	ds_read_b128 v[54:57], v138 offset:6160
	ds_read_b128 v[58:61], v138 offset:14336
	ds_read_b128 v[62:65], v138 offset:14352
	s_ashr_i32 s3, s2, 31
	v_lshlrev_b32_e32 v66, 3, v220
	s_lshl_b64 s[8:9], s[0:1], 12
	s_lshl_b64 s[2:3], s[2:3], 12
	v_or_b32_e32 v68, 0x400, v66
	v_or_b32_e32 v70, 0x600, v66
	s_add_u32 s10, s88, s2
	v_mov_b32_e32 v131, 0
	v_lshlrev_b32_e32 v1, 2, v1
	v_lshlrev_b32_e32 v130, 4, v220
	s_addc_u32 s11, s89, s3
	s_mov_b64 s[12:13], 0
	v_lshlrev_b32_e32 v139, 2, v66
	v_lshlrev_b32_e32 v140, 2, v68
	v_lshlrev_b32_e32 v141, 2, v70
	v_mov_b32_e32 v142, 0x3727c5ac
	s_mov_b32 s2, 0xf800000
	v_mov_b32_e32 v143, 0x260
	s_brev_b32 s3, 44
	s_mov_b32 s22, 0x38400000
	s_mov_b32 s23, s50
	s_mov_b32 s33, s23
	s_mov_b64 s[34:35], s[12:13]
	s_add_i32 s36, s33, 0xffffc000
	s_add_u32 s37, s50, s34
	s_addc_u32 s38, s51, s35
	s_cmpk_lt_i32 s33, 0x4000
	s_cselect_b32 s41, s38, 0
	s_cselect_b32 s40, s37, s36
	s_cselect_b32 s38, s17, s21
	s_cselect_b32 s37, s16, s20
	s_lshl_b64 s[40:41], s[40:41], 13
	s_add_u32 s44, s37, s40
	s_addc_u32 s45, s38, s41
	s_add_i32 s36, s92, s33
	s_cmpk_lt_i32 s36, 0x4400
	s_cselect_b32 s37, s36, s33
	s_ashr_i32 s40, s37, 31
	s_add_i32 s38, s37, 0xffffc000
	s_cmpk_lt_i32 s37, 0x4000
	s_cselect_b32 s41, s40, 0
	s_cselect_b32 s40, s37, s38
	s_cselect_b32 s39, s17, s21
	s_cselect_b32 s38, s16, s20
	s_lshl_b64 s[40:41], s[40:41], 13
	s_add_u32 s46, s38, s40
	s_addc_u32 s47, s39, s41
	global_load_dwordx4 v[170:173], v139, s[44:45] offset:16
	global_load_dwordx4 v[174:177], v139, s[44:45]
	global_load_dwordx4 v[178:181], v139, s[44:45] offset:2064
	global_load_dwordx4 v[182:185], v139, s[44:45] offset:2048
	global_load_dwordx4 v[186:189], v140, s[44:45] offset:16
	global_load_dwordx4 v[190:193], v140, s[44:45]
	global_load_dwordx4 v[196:199], v141, s[44:45] offset:16
	global_load_dwordx4 v[200:203], v141, s[44:45]
	global_load_dwordx4 v[204:207], v139, s[46:47] offset:16
	global_load_dwordx4 v[208:211], v139, s[46:47]
	global_load_dwordx4 v[212:215], v139, s[46:47] offset:2064
	global_load_dwordx4 v[216:219], v139, s[46:47] offset:2048
	global_load_dwordx4 v[224:227], v140, s[46:47] offset:16
	global_load_dwordx4 v[228:231], v140, s[46:47]
	global_load_dwordx4 v[232:235], v141, s[46:47] offset:16
	global_load_dwordx4 v[236:239], v141, s[46:47]
	s_waitcnt vmcnt(0)
	s_branch .Lmy_p0_entry
; #define LAS __attribute__((address_space(3)))
; __global__ void __launch_bounds__(NTHREADS, 2) fwd(Args args) {
;     ...
;             for (int t2 = 0; t2 < 2; ++t2) { const int m = m0 + t2 * NGW; if (m >= MR) break;
;                 const LAS float* shp = SHI + (m < T ? m / SEQ : 4) * D; const LAS float* scp = SCI + (m < T ? m / SEQ : 4) * D;
;                 f32x4 v[8]; float s = 0.f;
; #pragma unroll
;                 for (int j = 0; j < 8; ++j) { v[j] = vv[t2][j]; s += (v[j].x + v[j].y) + (v[j].z + v[j].w); }
;                 const float mean = wave_sum(s) * (1.f / D); float s2 = 0.f;
; #pragma unroll
;                 for (int j = 0; j < 8; ++j) { v[j] = v[j] - mean; s2 += (v[j].x * v[j].x + v[j].y * v[j].y) + (v[j].z * v[j].z + v[j].w * v[j].w); }
;                 const float rstd = 1.f / sqrtf(wave_sum(s2) * (1.f / D) + LN_EPS);
.LBB0_112:
	v_mov_b32_e32 v98, v94
	v_mov_b32_e32 v99, v90
	v_mov_b32_e32 v100, v95
	v_mov_b32_e32 v101, v91
	v_pk_add_f32 v[98:99], v[98:99], v[100:101]
	v_mov_b32_e32 v100, v96
	v_mov_b32_e32 v101, v92
	v_mov_b32_e32 v102, v97
	v_mov_b32_e32 v103, v93
	v_pk_add_f32 v[100:101], v[100:101], v[102:103]
	v_mov_b32_e32 v102, v86
	v_pk_add_f32 v[98:99], v[98:99], v[100:101]
	v_mov_b32_e32 v100, v87
	v_mov_b32_e32 v101, v88
	v_mov_b32_e32 v103, v89
	v_pk_add_f32 v[100:101], v[100:101], v[102:103]
	v_add_f32_e32 v98, 0, v98
	v_pk_add_f32 v[100:101], v[100:101], v[100:101] op_sel:[0,1] op_sel_hi:[1,0]
	v_add_f32_e32 v98, v98, v99
	v_add_f32_e32 v102, v82, v83
	v_add_f32_e32 v104, v84, v85
	v_mov_b32_e32 v99, v78
	v_mov_b32_e32 v101, v79
	v_mov_b32_e32 v103, v80
	v_mov_b32_e32 v105, v81
	v_pk_add_f32 v[98:99], v[98:99], v[100:101]
	v_pk_add_f32 v[100:101], v[102:103], v[104:105]
	v_mov_b32_e32 v102, v74
	v_pk_add_f32 v[98:99], v[98:99], v[100:101]
	v_mov_b32_e32 v100, v75
	v_mov_b32_e32 v101, v76
	v_mov_b32_e32 v103, v77
	v_pk_add_f32 v[100:101], v[100:101], v[102:103]
	v_pk_add_f32 v[98:99], v[98:99], v[98:99] op_sel:[0,1] op_sel_hi:[1,0]
	v_pk_add_f32 v[100:101], v[100:101], v[100:101] op_sel:[0,1] op_sel_hi:[1,0]
	v_add_f32_e32 v102, v70, v71
	v_add_f32_e32 v104, v72, v73
	v_mov_b32_e32 v99, v66
	v_mov_b32_e32 v101, v67
	v_mov_b32_e32 v103, v68
	v_mov_b32_e32 v105, v69
	v_pk_add_f32 v[98:99], v[98:99], v[100:101]
	v_pk_add_f32 v[100:101], v[102:103], v[104:105]
	v_lshl_add_u32 v146, s18, 2, v138
	v_pk_add_f32 v[98:99], v[98:99], v[100:101]
	s_nop 0
	v_add_f32_e32 v98, v98, v99
	ds_bpermute_b32 v99, v1, v98
	s_waitcnt lgkmcnt(0)
	v_add_f32_e32 v98, v98, v99
	ds_bpermute_b32 v99, v132, v98
	s_waitcnt lgkmcnt(0)
	v_add_f32_e32 v98, v98, v99
	ds_bpermute_b32 v99, v133, v98
	s_waitcnt lgkmcnt(0)
	v_add_f32_e32 v98, v98, v99
	ds_bpermute_b32 v99, v135, v98
	s_waitcnt lgkmcnt(0)
	v_add_f32_e32 v98, v98, v99
	ds_bpermute_b32 v99, v136, v98
	s_waitcnt lgkmcnt(0)
	v_add_f32_e32 v98, v98, v99
	ds_bpermute_b32 v99, v137, v98
	s_waitcnt lgkmcnt(0)
	v_add_f32_e32 v100, v98, v99
	v_fmamk_f32 v95, v100, 0xba000000, v95
	v_fmamk_f32 v91, v100, 0xba000000, v91
	v_fmamk_f32 v125, v100, 0xba000000, v97
	v_fmamk_f32 v124, v100, 0xba000000, v96
	v_fmac_f32_e32 v94, 0xba000000, v100
	v_fmamk_f32 v127, v100, 0xba000000, v93
	v_fmac_f32_e32 v90, 0xba000000, v100
	v_mov_b32_e32 v96, v95
	v_mov_b32_e32 v97, v91
	v_fmamk_f32 v126, v100, 0xba000000, v92
	v_mov_b32_e32 v92, v94
	v_mov_b32_e32 v93, v90
	v_pk_mul_f32 v[96:97], v[96:97], v[96:97]
	v_mov_b32_e32 v98, v125
	v_mov_b32_e32 v99, v127
	v_pk_fma_f32 v[92:93], v[92:93], v[92:93], v[96:97]
	v_mov_b32_e32 v96, v124
	v_mov_b32_e32 v97, v126
	v_pk_mul_f32 v[98:99], v[98:99], v[98:99]
	v_fmamk_f32 v129, v100, 0xba000000, v87
	v_pk_fma_f32 v[96:97], v[96:97], v[96:97], v[98:99]
	v_fmamk_f32 v128, v100, 0xba000000, v86
	v_fmamk_f32 v89, v100, 0xba000000, v89
	v_fmac_f32_e32 v88, 0xba000000, v100
	v_pk_add_f32 v[92:93], v[92:93], v[96:97]
	v_pk_mul_f32 v[86:87], v[88:89], v[88:89]
	v_pk_mul_f32 v[96:97], v[128:129], v[128:129]
	v_fmamk_f32 v79, v100, 0xba000000, v79
	v_pk_mov_b32 v[98:99], v[96:97], v[86:87] op_sel:[1,0]
	v_mov_b32_e32 v97, v87
	v_pk_add_f32 v[96:97], v[98:99], v[96:97]
	v_fmac_f32_e32 v78, 0xba000000, v100
	v_fmamk_f32 v87, v100, 0xba000000, v85
	v_fmamk_f32 v86, v100, 0xba000000, v84
	v_mul_f32_e32 v98, v78, v78
	v_mul_f32_e32 v99, v79, v79
	v_pk_add_f32 v[84:85], v[92:93], v[92:93] op_sel:[0,1] op_sel_hi:[1,0]
	v_pk_add_f32 v[92:93], v[96:97], v[96:97] op_sel:[0,1] op_sel_hi:[1,0]
	v_fmamk_f32 v83, v100, 0xba000000, v83
	v_mov_b32_e32 v85, v98
	v_mov_b32_e32 v93, v99
	v_fmac_f32_e32 v82, 0xba000000, v100
	v_fmamk_f32 v81, v100, 0xba000000, v81
	v_fmamk_f32 v80, v100, 0xba000000, v80
	v_pk_add_f32 v[84:85], v[84:85], v[92:93]
	v_mul_f32_e32 v92, v83, v83
	v_mul_f32_e32 v96, v87, v87
	v_mul_f32_e32 v101, v80, v80
	v_mul_f32_e32 v102, v81, v81
	v_pk_fma_f32 v[92:93], v[82:83], v[82:83], v[92:93] op_sel_hi:[1,1,0]
	v_pk_fma_f32 v[96:97], v[86:87], v[86:87], v[96:97] op_sel_hi:[1,1,0]
	v_mov_b32_e32 v93, v101
	v_mov_b32_e32 v97, v102
	v_pk_add_f32 v[92:93], v[92:93], v[96:97]
	v_fmamk_f32 v75, v100, 0xba000000, v75
	v_fmamk_f32 v74, v100, 0xba000000, v74
	v_fmamk_f32 v77, v100, 0xba000000, v77
	v_fmac_f32_e32 v76, 0xba000000, v100
	v_pk_add_f32 v[84:85], v[84:85], v[92:93]
	v_pk_mul_f32 v[92:93], v[76:77], v[76:77]
	v_pk_mul_f32 v[96:97], v[74:75], v[74:75]
	v_fmamk_f32 v67, v100, 0xba000000, v67
	v_pk_mov_b32 v[98:99], v[96:97], v[92:93] op_sel:[1,0]
	v_mov_b32_e32 v97, v93
	v_pk_add_f32 v[92:93], v[98:99], v[96:97]
	v_fmac_f32_e32 v66, 0xba000000, v100
	v_mul_f32_e32 v96, v66, v66
	v_mul_f32_e32 v97, v67, v67
	v_pk_add_f32 v[84:85], v[84:85], v[84:85] op_sel:[0,1] op_sel_hi:[1,0]
	v_pk_add_f32 v[92:93], v[92:93], v[92:93] op_sel:[0,1] op_sel_hi:[1,0]
	v_fmamk_f32 v73, v100, 0xba000000, v73
	v_fmamk_f32 v71, v100, 0xba000000, v71
	v_mov_b32_e32 v85, v96
	v_mov_b32_e32 v93, v97
	v_fmamk_f32 v72, v100, 0xba000000, v72
	v_fmac_f32_e32 v70, 0xba000000, v100
	v_fmamk_f32 v69, v100, 0xba000000, v69
	v_fmamk_f32 v68, v100, 0xba000000, v68
	v_pk_add_f32 v[84:85], v[84:85], v[92:93]
	v_mul_f32_e32 v92, v71, v71
	v_mul_f32_e32 v96, v73, v73
	v_mul_f32_e32 v98, v68, v68
	v_mul_f32_e32 v99, v69, v69
	v_pk_fma_f32 v[92:93], v[70:71], v[70:71], v[92:93] op_sel_hi:[1,1,0]
	v_pk_fma_f32 v[96:97], v[72:73], v[72:73], v[96:97] op_sel_hi:[1,1,0]
	v_mov_b32_e32 v93, v98
	v_mov_b32_e32 v97, v99
	v_pk_add_f32 v[92:93], v[92:93], v[96:97]
	s_nop 0
	v_pk_add_f32 v[84:85], v[84:85], v[92:93]
	s_nop 0
	v_add_f32_e32 v84, v84, v85
	ds_bpermute_b32 v85, v1, v84
	s_waitcnt lgkmcnt(0)
; #define LAS __attribute__((address_space(3)))
; __device__ __forceinline__ unsigned pk2(float lo, float hi) { const f32v2 v = {lo, hi}; return __builtin_bit_cast(unsigned, __builtin_convertvector(v, bf16v2)); }
; __global__ void __launch_bounds__(NTHREADS, 2) fwd(Args args) {
;     ...
;                 const float rstd = 1.f / sqrtf(wave_sum(s2) * (1.f / D) + LN_EPS);
; #pragma unroll
;                 for (int j2 = 0; j2 < 4; ++j2) { const int c8 = 8 * (lane + 64 * j2); u32x4 on, om;
; #pragma unroll
;                     for (int hf = 0; hf < 2; ++hf) { const int j = 2 * j2 + hf, c = c8 + 4 * hf; const f32x4 g = *(const LAS f32x4*)(LGI + c), bb = *(const LAS f32x4*)(LBI + c);
;                         f32x4 hh; hh.x = v[j].x * rstd * g.x + bb.x; hh.y = v[j].y * rstd * g.y + bb.y; hh.z = v[j].z * rstd * g.z + bb.z; hh.w = v[j].w * rstd * g.w + bb.w;
;                         const f32x4 s4 = *(const LAS f32x4*)(shp + c), c4 = *(const LAS f32x4*)(scp + c);
;                         const unsigned n0 = pk2(hh.x, hh.y), n1 = pk2(hh.z, hh.w), m0_ = pk2(hh.x * (1.f + c4.x) + s4.x, hh.y * (1.f + c4.y) + s4.y), m1_ = pk2(hh.z * (1.f + c4.z) + s4.z, hh.w * (1.f + c4.w) + s4.w);
;                         if (hf == 0) { on.x = n0; on.y = n1; om.x = m0_; om.y = m1_; } else { on.z = n0; on.w = n1; om.z = m0_; om.w = m1_; } }
;                     *(u32x4*)(HN + (size_t)m * D + c8) = on; *(u32x4*)(HM + (size_t)m * D + c8) = om; }
	v_add_f32_e32 v84, v84, v85
	ds_bpermute_b32 v85, v132, v84
	s_waitcnt lgkmcnt(0)
	v_add_f32_e32 v84, v84, v85
	ds_bpermute_b32 v85, v133, v84
	s_waitcnt lgkmcnt(0)
	v_add_f32_e32 v84, v84, v85
	ds_bpermute_b32 v85, v135, v84
	s_waitcnt lgkmcnt(0)
	v_add_f32_e32 v84, v84, v85
	ds_bpermute_b32 v85, v136, v84
	s_waitcnt lgkmcnt(0)
	v_add_f32_e32 v84, v84, v85
	ds_bpermute_b32 v85, v137, v84
	s_waitcnt lgkmcnt(0)
	v_add_f32_e32 v84, v84, v85
	v_fmamk_f32 v84, v84, 0x3a000000, v142
	v_mul_f32_e32 v85, 0x4f800000, v84
	v_cmp_gt_f32_e32 vcc, s2, v84
	s_nop 1
	v_cndmask_b32_e32 v84, v84, v85, vcc
	v_sqrt_f32_e32 v85, v84
	s_nop 0
	v_add_u32_e32 v92, -1, v85
	v_fma_f32 v93, -v92, v85, v84
	v_cmp_ge_f32_e64 s[6:7], 0, v93
	v_add_u32_e32 v93, 1, v85
	s_nop 0
	v_cndmask_b32_e64 v92, v85, v92, s[6:7]
	v_fma_f32 v85, -v93, v85, v84
	v_cmp_lt_f32_e64 s[6:7], 0, v85
	s_nop 1
	v_cndmask_b32_e64 v85, v92, v93, s[6:7]
	v_mul_f32_e32 v92, 0x37800000, v85
	v_cndmask_b32_e32 v85, v85, v92, vcc
	v_cmp_class_f32_e32 vcc, v84, v143
	s_nop 1
	v_cndmask_b32_e32 v84, v85, v84, vcc
	v_div_scale_f32 v85, s[6:7], v84, v84, 1.0
	v_rcp_f32_e32 v92, v85
	s_nop 0
	v_fma_f32 v93, -v85, v92, 1.0
	v_fmac_f32_e32 v92, v93, v92
	v_div_scale_f32 v93, vcc, 1.0, v84, 1.0
	v_mul_f32_e32 v96, v93, v92
	v_fma_f32 v97, -v85, v96, v93
	v_fmac_f32_e32 v96, v97, v92
	v_fma_f32 v85, -v85, v96, v93
	v_div_fmas_f32 v85, v85, v92, v96
	v_div_fixup_f32 v84, v85, v84, 1.0
	ds_read_b128 v[96:99], v138
	ds_read_b128 v[100:103], v138 offset:16
	ds_read_b128 v[104:107], v138 offset:8192
	v_lshl_add_u32 v85, s19, 2, v138
	ds_read_b128 v[108:111], v85 offset:16384
	ds_read_b128 v[112:115], v85 offset:16400
	ds_read_b128 v[116:119], v146 offset:57344
	ds_read_b128 v[120:123], v146 offset:57360
	v_pk_mul_f32 v[144:145], v[84:85], v[94:95] op_sel_hi:[0,1]
	ds_read_b128 v[92:95], v138 offset:8208
	s_waitcnt lgkmcnt(5)
	v_pk_fma_f32 v[104:105], v[96:97], v[144:145], v[104:105]
	s_waitcnt lgkmcnt(2)
	v_pk_add_f32 v[116:117], v[116:117], 1.0 op_sel_hi:[1,0]
	v_cvt_pk_bf16_f32 v96, v104, v105
	v_pk_fma_f32 v[104:105], v[104:105], v[116:117], v[108:109]
	v_pk_mul_f32 v[108:109], v[84:85], v[124:125] op_sel_hi:[0,1]
	v_pk_fma_f32 v[98:99], v[98:99], v[108:109], v[106:107]
	v_pk_add_f32 v[106:107], v[118:119], 1.0 op_sel_hi:[1,0]
	v_pk_mul_f32 v[90:91], v[84:85], v[90:91] op_sel_hi:[0,1]
	v_cvt_pk_bf16_f32 v97, v98, v99
	v_pk_fma_f32 v[98:99], v[98:99], v[106:107], v[110:111]
	s_waitcnt lgkmcnt(0)
	v_pk_fma_f32 v[90:91], v[100:101], v[90:91], v[92:93]
	v_pk_add_f32 v[92:93], v[120:121], 1.0 op_sel_hi:[1,0]
	v_cvt_pk_bf16_f32 v104, v104, v105
	v_cvt_pk_bf16_f32 v105, v98, v99
	v_cvt_pk_bf16_f32 v98, v90, v91
	v_pk_fma_f32 v[90:91], v[90:91], v[92:93], v[112:113]
	v_pk_add_f32 v[92:93], v[122:123], 1.0 op_sel_hi:[1,0]
	v_cvt_pk_bf16_f32 v106, v90, v91
	v_pk_mul_f32 v[90:91], v[84:85], v[126:127] op_sel_hi:[0,1]
	v_pk_fma_f32 v[90:91], v[102:103], v[90:91], v[94:95]
	v_pk_mul_f32 v[88:89], v[84:85], v[88:89] op_sel_hi:[0,1]
	v_cvt_pk_bf16_f32 v99, v90, v91
	v_pk_fma_f32 v[90:91], v[90:91], v[92:93], v[114:115]
	v_pk_mul_f32 v[114:115], v[84:85], v[128:129] op_sel_hi:[0,1]
	v_cvt_pk_bf16_f32 v107, v90, v91
	v_lshl_add_u64 v[90:91], s[10:11], 0, v[130:131]
	v_add_co_u32_e32 v122, vcc, s3, v90
	v_pk_mul_f32 v[82:83], v[84:85], v[82:83] op_sel_hi:[0,1]
	s_nop 0
	v_addc_co_u32_e32 v123, vcc, 0, v91, vcc
	v_add_co_u32_e32 v124, vcc, s22, v90
	global_store_dwordx4 v[122:123], v[96:99], off
	s_nop 0
	v_addc_co_u32_e32 v125, vcc, 0, v91, vcc
	global_store_dwordx4 v[124:125], v[104:107], off
	ds_read_b128 v[90:93], v138 offset:2048
	ds_read_b128 v[94:97], v138 offset:10240
	ds_read_b128 v[98:101], v85 offset:18432
	ds_read_b128 v[102:105], v146 offset:59392
	ds_read_b128 v[106:109], v138 offset:2064
	ds_read_b128 v[110:113], v138 offset:10256
	ds_read_b128 v[118:121], v85 offset:18448
	s_waitcnt lgkmcnt(5)
	v_pk_fma_f32 v[94:95], v[90:91], v[114:115], v[94:95]
	ds_read_b128 v[114:117], v146 offset:59408
	s_waitcnt lgkmcnt(4)
	v_pk_add_f32 v[102:103], v[102:103], 1.0 op_sel_hi:[1,0]
	v_pk_fma_f32 v[88:89], v[92:93], v[88:89], v[96:97]
	v_pk_add_f32 v[92:93], v[104:105], 1.0 op_sel_hi:[1,0]
	v_cvt_pk_bf16_f32 v90, v94, v95
	v_pk_fma_f32 v[94:95], v[94:95], v[102:103], v[98:99]
	v_cvt_pk_bf16_f32 v91, v88, v89
	v_pk_fma_f32 v[88:89], v[88:89], v[92:93], v[100:101]
	v_cvt_pk_bf16_f32 v94, v94, v95
	v_cvt_pk_bf16_f32 v95, v88, v89
	s_waitcnt lgkmcnt(2)
; #define LAS __attribute__((address_space(3)))
; __device__ __forceinline__ unsigned pk2(float lo, float hi) { const f32v2 v = {lo, hi}; return __builtin_bit_cast(unsigned, __builtin_convertvector(v, bf16v2)); }
; __global__ void __launch_bounds__(NTHREADS, 2) fwd(Args args) {
;     ...
; #pragma unroll
;                 for (int j2 = 0; j2 < 4; ++j2) { const int c8 = 8 * (lane + 64 * j2); u32x4 on, om;
; #pragma unroll
;                     for (int hf = 0; hf < 2; ++hf) { const int j = 2 * j2 + hf, c = c8 + 4 * hf; const f32x4 g = *(const LAS f32x4*)(LGI + c), bb = *(const LAS f32x4*)(LBI + c);
;                         f32x4 hh; hh.x = v[j].x * rstd * g.x + bb.x; hh.y = v[j].y * rstd * g.y + bb.y; hh.z = v[j].z * rstd * g.z + bb.z; hh.w = v[j].w * rstd * g.w + bb.w;
;                         const f32x4 s4 = *(const LAS f32x4*)(shp + c), c4 = *(const LAS f32x4*)(scp + c);
;                         const unsigned n0 = pk2(hh.x, hh.y), n1 = pk2(hh.z, hh.w), m0_ = pk2(hh.x * (1.f + c4.x) + s4.x, hh.y * (1.f + c4.y) + s4.y), m1_ = pk2(hh.z * (1.f + c4.z) + s4.z, hh.w * (1.f + c4.w) + s4.w);
;                         if (hf == 0) { on.x = n0; on.y = n1; om.x = m0_; om.y = m1_; } else { on.z = n0; on.w = n1; om.z = m0_; om.w = m1_; } }
;                     *(u32x4*)(HN + (size_t)m * D + c8) = on; *(u32x4*)(HM + (size_t)m * D + c8) = om; }
	v_pk_fma_f32 v[82:83], v[106:107], v[82:83], v[110:111]
	s_waitcnt lgkmcnt(0)
	v_pk_add_f32 v[88:89], v[114:115], 1.0 op_sel_hi:[1,0]
	v_cvt_pk_bf16_f32 v92, v82, v83
	v_pk_fma_f32 v[82:83], v[82:83], v[88:89], v[118:119]
	v_pk_mul_f32 v[78:79], v[84:85], v[78:79] op_sel_hi:[0,1]
	v_cvt_pk_bf16_f32 v96, v82, v83
	v_pk_mul_f32 v[82:83], v[84:85], v[86:87] op_sel_hi:[0,1]
	v_pk_fma_f32 v[82:83], v[108:109], v[82:83], v[112:113]
	v_pk_add_f32 v[86:87], v[116:117], 1.0 op_sel_hi:[1,0]
	v_cvt_pk_bf16_f32 v93, v82, v83
	v_pk_fma_f32 v[82:83], v[82:83], v[86:87], v[120:121]
	v_pk_mul_f32 v[80:81], v[84:85], v[80:81] op_sel_hi:[0,1]
	v_cvt_pk_bf16_f32 v97, v82, v83
	global_store_dwordx4 v[122:123], v[90:93], off offset:1024
	global_store_dwordx4 v[124:125], v[94:97], off offset:1024
	ds_read_b128 v[86:89], v138 offset:4096
	ds_read_b128 v[90:93], v138 offset:4112
	ds_read_b128 v[94:97], v138 offset:12288
	ds_read_b128 v[98:101], v85 offset:20480
	ds_read_b128 v[102:105], v85 offset:20496
	ds_read_b128 v[106:109], v146 offset:61440
	ds_read_b128 v[110:113], v146 offset:61456
	ds_read_b128 v[114:117], v138 offset:12304
	s_waitcnt lgkmcnt(5)
	v_pk_fma_f32 v[82:83], v[86:87], v[78:79], v[94:95]
	v_pk_fma_f32 v[80:81], v[88:89], v[80:81], v[96:97]
	s_waitcnt lgkmcnt(2)
	v_pk_add_f32 v[86:87], v[106:107], 1.0 op_sel_hi:[1,0]
	v_cvt_pk_bf16_f32 v78, v82, v83
	v_pk_fma_f32 v[82:83], v[82:83], v[86:87], v[98:99]
	v_pk_mul_f32 v[74:75], v[84:85], v[74:75] op_sel_hi:[0,1]
	v_cvt_pk_bf16_f32 v86, v82, v83
	v_pk_add_f32 v[82:83], v[108:109], 1.0 op_sel_hi:[1,0]
	v_cvt_pk_bf16_f32 v79, v80, v81
	v_pk_fma_f32 v[80:81], v[80:81], v[82:83], v[100:101]
	s_waitcnt lgkmcnt(0)
	v_pk_fma_f32 v[74:75], v[90:91], v[74:75], v[114:115]
	v_pk_add_f32 v[82:83], v[110:111], 1.0 op_sel_hi:[1,0]
	v_cvt_pk_bf16_f32 v87, v80, v81
	v_cvt_pk_bf16_f32 v80, v74, v75
	v_pk_fma_f32 v[74:75], v[74:75], v[82:83], v[102:103]
	v_pk_mul_f32 v[70:71], v[84:85], v[70:71] op_sel_hi:[0,1]
	v_cvt_pk_bf16_f32 v88, v74, v75
	v_pk_mul_f32 v[74:75], v[84:85], v[76:77] op_sel_hi:[0,1]
	v_pk_fma_f32 v[74:75], v[92:93], v[74:75], v[116:117]
	v_pk_add_f32 v[76:77], v[112:113], 1.0 op_sel_hi:[1,0]
	v_cvt_pk_bf16_f32 v81, v74, v75
	v_pk_fma_f32 v[74:75], v[74:75], v[76:77], v[104:105]
	v_pk_mul_f32 v[72:73], v[84:85], v[72:73] op_sel_hi:[0,1]
	v_cvt_pk_bf16_f32 v89, v74, v75
	global_store_dwordx4 v[122:123], v[78:81], off offset:2048
	global_store_dwordx4 v[124:125], v[86:89], off offset:2048
	ds_read_b128 v[74:77], v138 offset:6144
	ds_read_b128 v[78:81], v138 offset:14336
	ds_read_b128 v[86:89], v85 offset:22528
	ds_read_b128 v[90:93], v146 offset:63488
	ds_read_b128 v[94:97], v138 offset:6160
	ds_read_b128 v[98:101], v138 offset:14352
	ds_read_b128 v[102:105], v146 offset:63504
	ds_read_b128 v[106:109], v85 offset:22544
	s_waitcnt lgkmcnt(6)
	v_pk_fma_f32 v[74:75], v[74:75], v[70:71], v[78:79]
	s_waitcnt lgkmcnt(4)
	v_pk_add_f32 v[78:79], v[90:91], 1.0 op_sel_hi:[1,0]
	v_pk_fma_f32 v[72:73], v[76:77], v[72:73], v[80:81]
	v_pk_add_f32 v[76:77], v[92:93], 1.0 op_sel_hi:[1,0]
	v_pk_mul_f32 v[66:67], v[84:85], v[66:67] op_sel_hi:[0,1]
	v_cvt_pk_bf16_f32 v70, v74, v75
	v_pk_fma_f32 v[74:75], v[74:75], v[78:79], v[86:87]
	v_cvt_pk_bf16_f32 v71, v72, v73
	v_pk_fma_f32 v[72:73], v[72:73], v[76:77], v[88:89]
	s_waitcnt lgkmcnt(2)
	v_pk_fma_f32 v[66:67], v[94:95], v[66:67], v[98:99]
	s_waitcnt lgkmcnt(1)
	v_pk_add_f32 v[76:77], v[102:103], 1.0 op_sel_hi:[1,0]
	v_cvt_pk_bf16_f32 v74, v74, v75
	v_cvt_pk_bf16_f32 v75, v72, v73
	v_cvt_pk_bf16_f32 v72, v66, v67
	s_waitcnt lgkmcnt(0)
	v_pk_fma_f32 v[66:67], v[66:67], v[76:77], v[106:107]
	s_nop 0
	v_cvt_pk_bf16_f32 v76, v66, v67
	v_pk_mul_f32 v[66:67], v[84:85], v[68:69] op_sel_hi:[0,1]
	v_pk_fma_f32 v[66:67], v[96:97], v[66:67], v[100:101]
	v_pk_add_f32 v[68:69], v[104:105], 1.0 op_sel_hi:[1,0]
	v_cvt_pk_bf16_f32 v73, v66, v67
	v_pk_fma_f32 v[66:67], v[66:67], v[68:69], v[108:109]
	s_nop 0
	v_cvt_pk_bf16_f32 v77, v66, v67
	global_store_dwordx4 v[122:123], v[70:73], off offset:3072
	global_store_dwordx4 v[124:125], v[74:77], off offset:3072

; __global__ void __launch_bounds__(NTHREADS, 2) fwd(Args args) {
;     ...
;         for (int m0 = gw; m0 < MR; m0 += 2 * NGW) {
;             f32x4 vv[2][8];
; #pragma unroll
;             for (int t2 = 0; t2 < 2; ++t2) { const int m = (m0 + t2 * NGW) < MR ? m0 + t2 * NGW : m0; const float* xr = m < T ? x + (size_t)m * D : ctx + (size_t)(m - T) * D;
; #pragma unroll
;                 for (int j = 0; j < 8; ++j) vv[t2][j] = *(const f32x4*)(xr + 8 * (lane + 64 * (j >> 1)) + 4 * (j & 1)); }
.LBB0_114:
	s_waitcnt vmcnt(16)
.Lmy_p0_entry:
	s_add_i32 s24, s23, 0xffffc000
	s_add_u32 s25, s50, s12
	s_addc_u32 s26, s51, s13
	s_cmpk_lt_i32 s23, 0x4000
	s_cselect_b64 s[6:7], -1, 0
	s_and_b64 s[18:19], s[6:7], exec
	s_cselect_b32 s19, s26, 0
	s_cselect_b32 s18, s25, s24
	s_cselect_b32 s24, s17, s21
	s_cselect_b32 s25, s16, s20
	s_lshl_b64 s[18:19], s[18:19], 13
	s_add_u32 s26, s25, s18
	s_addc_u32 s27, s24, s19
	s_add_i32 s24, s92, s23
	s_cmpk_lt_i32 s24, 0x4400
	s_cselect_b64 s[18:19], -1, 0
	s_and_b64 s[28:29], s[18:19], exec
	s_cselect_b32 s25, s24, s23
	s_ashr_i32 s28, s25, 31
	s_add_i32 s30, s25, 0xffffc000
	s_cmpk_lt_i32 s25, 0x4000
	s_cselect_b32 s29, s28, 0
	s_cselect_b32 s28, s25, s30
	s_cselect_b32 s25, s17, s21
	s_cselect_b32 s30, s16, s20
	s_lshl_b64 s[28:29], s[28:29], 13
	s_add_u32 s28, s30, s28
	s_addc_u32 s29, s25, s29
	v_mov_b64_e32 v[122:123], v[170:171]
	v_mov_b64_e32 v[124:125], v[172:173]
	v_mov_b64_e32 v[126:127], v[174:175]
	v_mov_b64_e32 v[128:129], v[176:177]
	v_mov_b64_e32 v[114:115], v[178:179]
	v_mov_b64_e32 v[116:117], v[180:181]
	v_mov_b64_e32 v[118:119], v[182:183]
	v_mov_b64_e32 v[120:121], v[184:185]
	v_mov_b64_e32 v[106:107], v[186:187]
	v_mov_b64_e32 v[108:109], v[188:189]
	v_mov_b64_e32 v[110:111], v[190:191]
	v_mov_b64_e32 v[112:113], v[192:193]
	v_mov_b64_e32 v[98:99], v[196:197]
	v_mov_b64_e32 v[100:101], v[198:199]
	v_mov_b64_e32 v[102:103], v[200:201]
	v_mov_b64_e32 v[104:105], v[202:203]
	v_mov_b64_e32 v[90:91], v[204:205]
	v_mov_b64_e32 v[92:93], v[206:207]
	v_mov_b64_e32 v[94:95], v[208:209]
	v_mov_b64_e32 v[96:97], v[210:211]
	v_mov_b64_e32 v[82:83], v[212:213]
	v_mov_b64_e32 v[84:85], v[214:215]
	v_mov_b64_e32 v[86:87], v[216:217]
	v_mov_b64_e32 v[88:89], v[218:219]
	v_mov_b64_e32 v[74:75], v[224:225]
	v_mov_b64_e32 v[76:77], v[226:227]
	v_mov_b64_e32 v[78:79], v[228:229]
	v_mov_b64_e32 v[80:81], v[230:231]
	v_mov_b64_e32 v[66:67], v[232:233]
	v_mov_b64_e32 v[68:69], v[234:235]
	v_mov_b64_e32 v[70:71], v[236:237]
	v_mov_b64_e32 v[72:73], v[238:239]
	s_add_i32 s33, s23, s0
	s_add_u32 s34, s12, s0
	s_addc_u32 s35, s13, s1
	s_cmpk_lt_i32 s33, 0x4400
	s_cbranch_scc0 .Lmy_p0_noload
	s_add_i32 s36, s33, 0xffffc000
	s_add_u32 s37, s50, s34
	s_addc_u32 s38, s51, s35
	s_cmpk_lt_i32 s33, 0x4000
	s_cselect_b32 s41, s38, 0
	s_cselect_b32 s40, s37, s36
	s_cselect_b32 s38, s17, s21
	s_cselect_b32 s37, s16, s20
	s_lshl_b64 s[40:41], s[40:41], 13
	s_add_u32 s44, s37, s40
	s_addc_u32 s45, s38, s41
	s_add_i32 s36, s92, s33
	s_cmpk_lt_i32 s36, 0x4400
	s_cselect_b32 s37, s36, s33
	s_ashr_i32 s40, s37, 31
	s_add_i32 s38, s37, 0xffffc000
	s_cmpk_lt_i32 s37, 0x4000
	s_cselect_b32 s41, s40, 0
	s_cselect_b32 s40, s37, s38
	s_cselect_b32 s39, s17, s21
	s_cselect_b32 s38, s16, s20
	s_lshl_b64 s[40:41], s[40:41], 13
	s_add_u32 s46, s38, s40
	s_addc_u32 s47, s39, s41
	global_load_dwordx4 v[170:173], v139, s[44:45] offset:16
	global_load_dwordx4 v[174:177], v139, s[44:45]
	global_load_dwordx4 v[178:181], v139, s[44:45] offset:2064
	global_load_dwordx4 v[182:185], v139, s[44:45] offset:2048
	global_load_dwordx4 v[186:189], v140, s[44:45] offset:16
	global_load_dwordx4 v[190:193], v140, s[44:45]
	global_load_dwordx4 v[196:199], v141, s[44:45] offset:16
	global_load_dwordx4 v[200:203], v141, s[44:45]
	global_load_dwordx4 v[204:207], v139, s[46:47] offset:16
	global_load_dwordx4 v[208:211], v139, s[46:47]
	global_load_dwordx4 v[212:215], v139, s[46:47] offset:2064
	global_load_dwordx4 v[216:219], v139, s[46:47] offset:2048
	global_load_dwordx4 v[224:227], v140, s[46:47] offset:16
	global_load_dwordx4 v[228:231], v140, s[46:47]
	global_load_dwordx4 v[232:235], v141, s[46:47] offset:16
	global_load_dwordx4 v[236:239], v141, s[46:47]
.Lmy_p0_noload:
	s_cmpk_gt_i32 s23, 0x3fff
	s_movk_i32 s25, 0x2000
	s_movk_i32 s26, 0x2000
	s_cbranch_scc1 .LBB0_116
	s_ashr_i32 s26, s23, 31
	s_lshr_b32 s26, s26, 20
	s_add_i32 s26, s23, s26
	s_ashr_i32 s26, s26, 12
	s_lshl_b32 s26, s26, 11

; #define LAS __attribute__((address_space(3)))
; __global__ void __launch_bounds__(NTHREADS, 2) fwd(Args args) {
;     ...
;             for (int t2 = 0; t2 < 2; ++t2) { const int m = m0 + t2 * NGW; if (m >= MR) break;
;                 const LAS float* shp = SHI + (m < T ? m / SEQ : 4) * D; const LAS float* scp = SCI + (m < T ? m / SEQ : 4) * D;
;                 f32x4 v[8]; float s = 0.f;
; #pragma unroll
;                 for (int j = 0; j < 8; ++j) { v[j] = vv[t2][j]; s += (v[j].x + v[j].y) + (v[j].z + v[j].w); }
;                 const float mean = wave_sum(s) * (1.f / D); float s2 = 0.f;
; #pragma unroll
;                 for (int j = 0; j < 8; ++j) { v[j] = v[j] - mean; s2 += (v[j].x * v[j].x + v[j].y * v[j].y) + (v[j].z * v[j].z + v[j].w * v[j].w); }
;                 const float rstd = 1.f / sqrtf(wave_sum(s2) * (1.f / D) + LN_EPS);
.LBB0_118:
	v_mov_b32_e32 v144, v126
	v_mov_b32_e32 v145, v122
	v_mov_b32_e32 v146, v127
	v_mov_b32_e32 v147, v123
	v_pk_add_f32 v[144:145], v[144:145], v[146:147]
	v_mov_b32_e32 v146, v128
	v_mov_b32_e32 v147, v124
	v_mov_b32_e32 v148, v129
	v_mov_b32_e32 v149, v125
	v_pk_add_f32 v[146:147], v[146:147], v[148:149]
	v_mov_b32_e32 v148, v118
	v_pk_add_f32 v[144:145], v[144:145], v[146:147]
	v_mov_b32_e32 v146, v119
	v_mov_b32_e32 v147, v120
	v_mov_b32_e32 v149, v121
	v_pk_add_f32 v[146:147], v[146:147], v[148:149]
	v_add_f32_e32 v144, 0, v144
	v_pk_add_f32 v[146:147], v[146:147], v[146:147] op_sel:[0,1] op_sel_hi:[1,0]
	v_add_f32_e32 v144, v144, v145
	v_add_f32_e32 v148, v114, v115
	v_add_f32_e32 v150, v116, v117
	v_mov_b32_e32 v145, v110
	v_mov_b32_e32 v147, v111
	v_mov_b32_e32 v149, v112
	v_mov_b32_e32 v151, v113
	v_pk_add_f32 v[144:145], v[144:145], v[146:147]
	v_pk_add_f32 v[146:147], v[148:149], v[150:151]
	v_mov_b32_e32 v148, v106
	v_pk_add_f32 v[144:145], v[144:145], v[146:147]
	v_mov_b32_e32 v146, v107
	v_mov_b32_e32 v147, v108
	v_mov_b32_e32 v149, v109
	v_pk_add_f32 v[146:147], v[146:147], v[148:149]
	v_pk_add_f32 v[144:145], v[144:145], v[144:145] op_sel:[0,1] op_sel_hi:[1,0]
	v_pk_add_f32 v[146:147], v[146:147], v[146:147] op_sel:[0,1] op_sel_hi:[1,0]
	v_add_f32_e32 v148, v102, v103
	v_add_f32_e32 v150, v104, v105
	v_mov_b32_e32 v145, v98
	v_mov_b32_e32 v147, v99
	v_mov_b32_e32 v149, v100
	v_mov_b32_e32 v151, v101
	v_pk_add_f32 v[144:145], v[144:145], v[146:147]
	v_pk_add_f32 v[146:147], v[148:149], v[150:151]
	v_lshl_add_u32 v163, s26, 2, v138
	v_pk_add_f32 v[144:145], v[144:145], v[146:147]
	v_lshl_add_u32 v164, s25, 2, v138
	v_add_f32_e32 v144, v144, v145
	ds_bpermute_b32 v145, v1, v144
	s_waitcnt lgkmcnt(0)
	v_add_f32_e32 v144, v144, v145
	ds_bpermute_b32 v145, v132, v144
	s_waitcnt lgkmcnt(0)
	v_add_f32_e32 v144, v144, v145
	ds_bpermute_b32 v145, v133, v144
	s_waitcnt lgkmcnt(0)
	v_add_f32_e32 v144, v144, v145
	ds_bpermute_b32 v145, v135, v144
	s_waitcnt lgkmcnt(0)
	v_add_f32_e32 v144, v144, v145
	ds_bpermute_b32 v145, v136, v144
	s_waitcnt lgkmcnt(0)
	v_add_f32_e32 v144, v144, v145
	ds_bpermute_b32 v145, v137, v144
	s_waitcnt lgkmcnt(0)
	v_add_f32_e32 v148, v144, v145
	v_fmamk_f32 v127, v148, 0xba000000, v127
	v_fmamk_f32 v123, v148, 0xba000000, v123
	v_fmamk_f32 v129, v148, 0xba000000, v129
	v_fmac_f32_e32 v126, 0xba000000, v148
	v_fmamk_f32 v157, v148, 0xba000000, v125
	v_fmac_f32_e32 v122, 0xba000000, v148
	v_mov_b32_e32 v144, v127
	v_mov_b32_e32 v145, v123
	v_fmamk_f32 v128, v148, 0xba000000, v128
	v_fmamk_f32 v156, v148, 0xba000000, v124
	v_mov_b32_e32 v124, v126
	v_mov_b32_e32 v125, v122
	v_pk_mul_f32 v[144:145], v[144:145], v[144:145]
	v_mov_b32_e32 v146, v129
	v_mov_b32_e32 v147, v157
	v_pk_fma_f32 v[124:125], v[124:125], v[124:125], v[144:145]
	v_mov_b32_e32 v144, v128
	v_mov_b32_e32 v145, v156
	v_pk_mul_f32 v[146:147], v[146:147], v[146:147]
	v_fmamk_f32 v159, v148, 0xba000000, v119
	v_pk_fma_f32 v[144:145], v[144:145], v[144:145], v[146:147]
	v_fmamk_f32 v158, v148, 0xba000000, v118
	v_fmamk_f32 v121, v148, 0xba000000, v121
	v_fmac_f32_e32 v120, 0xba000000, v148
	v_pk_add_f32 v[124:125], v[124:125], v[144:145]
	v_pk_mul_f32 v[118:119], v[120:121], v[120:121]
	v_pk_mul_f32 v[144:145], v[158:159], v[158:159]
	v_fmamk_f32 v111, v148, 0xba000000, v111
	v_pk_mov_b32 v[146:147], v[144:145], v[118:119] op_sel:[1,0]
	v_mov_b32_e32 v145, v119
	v_pk_add_f32 v[118:119], v[146:147], v[144:145]
	v_fmac_f32_e32 v110, 0xba000000, v148
	v_fmamk_f32 v161, v148, 0xba000000, v117
	v_fmamk_f32 v160, v148, 0xba000000, v116
	v_mul_f32_e32 v144, v110, v110
	v_mul_f32_e32 v145, v111, v111
	v_pk_add_f32 v[116:117], v[124:125], v[124:125] op_sel:[0,1] op_sel_hi:[1,0]
	v_pk_add_f32 v[118:119], v[118:119], v[118:119] op_sel:[0,1] op_sel_hi:[1,0]
	v_fmamk_f32 v115, v148, 0xba000000, v115
	v_mov_b32_e32 v117, v144
	v_mov_b32_e32 v119, v145
	v_fmac_f32_e32 v114, 0xba000000, v148
	v_fmamk_f32 v113, v148, 0xba000000, v113
	v_fmamk_f32 v112, v148, 0xba000000, v112
	v_pk_add_f32 v[116:117], v[116:117], v[118:119]
	v_mul_f32_e32 v118, v115, v115
	v_mul_f32_e32 v124, v161, v161
	v_mul_f32_e32 v146, v112, v112
	v_mul_f32_e32 v147, v113, v113
	v_pk_fma_f32 v[118:119], v[114:115], v[114:115], v[118:119] op_sel_hi:[1,1,0]
	v_pk_fma_f32 v[124:125], v[160:161], v[160:161], v[124:125] op_sel_hi:[1,1,0]
	v_mov_b32_e32 v119, v146
	v_mov_b32_e32 v125, v147
	v_pk_add_f32 v[118:119], v[118:119], v[124:125]
	v_fmamk_f32 v107, v148, 0xba000000, v107
	v_fmamk_f32 v106, v148, 0xba000000, v106
	v_fmamk_f32 v109, v148, 0xba000000, v109
	v_fmac_f32_e32 v108, 0xba000000, v148
	v_pk_add_f32 v[116:117], v[116:117], v[118:119]
	v_pk_mul_f32 v[118:119], v[108:109], v[108:109]
	v_pk_mul_f32 v[124:125], v[106:107], v[106:107]
	v_fmamk_f32 v99, v148, 0xba000000, v99
	v_pk_mov_b32 v[144:145], v[124:125], v[118:119] op_sel:[1,0]
	v_mov_b32_e32 v125, v119
	v_pk_add_f32 v[118:119], v[144:145], v[124:125]
	v_fmac_f32_e32 v98, 0xba000000, v148
	v_mul_f32_e32 v124, v98, v98
	v_mul_f32_e32 v125, v99, v99
	v_pk_add_f32 v[116:117], v[116:117], v[116:117] op_sel:[0,1] op_sel_hi:[1,0]
	v_pk_add_f32 v[118:119], v[118:119], v[118:119] op_sel:[0,1] op_sel_hi:[1,0]
	v_fmamk_f32 v105, v148, 0xba000000, v105
	v_fmamk_f32 v103, v148, 0xba000000, v103
	v_mov_b32_e32 v117, v124
	v_mov_b32_e32 v119, v125
	v_fmamk_f32 v104, v148, 0xba000000, v104
	v_fmac_f32_e32 v102, 0xba000000, v148
	v_fmamk_f32 v101, v148, 0xba000000, v101
	v_fmamk_f32 v100, v148, 0xba000000, v100
	v_pk_add_f32 v[116:117], v[116:117], v[118:119]
	v_mul_f32_e32 v118, v103, v103
	v_mul_f32_e32 v124, v105, v105
	v_mul_f32_e32 v144, v100, v100
	v_mul_f32_e32 v145, v101, v101
	v_pk_fma_f32 v[118:119], v[102:103], v[102:103], v[118:119] op_sel_hi:[1,1,0]
	v_pk_fma_f32 v[124:125], v[104:105], v[104:105], v[124:125] op_sel_hi:[1,1,0]
	v_mov_b32_e32 v119, v144
	v_mov_b32_e32 v125, v145
	v_pk_add_f32 v[118:119], v[118:119], v[124:125]
	s_nop 0
	v_pk_add_f32 v[116:117], v[116:117], v[118:119]
	s_nop 0
	v_add_f32_e32 v116, v116, v117
	ds_bpermute_b32 v117, v1, v116
	s_waitcnt lgkmcnt(0)
; #define LAS __attribute__((address_space(3)))
; __device__ __forceinline__ unsigned pk2(float lo, float hi) { const f32v2 v = {lo, hi}; return __builtin_bit_cast(unsigned, __builtin_convertvector(v, bf16v2)); }
; __global__ void __launch_bounds__(NTHREADS, 2) fwd(Args args) {
;     ...
;                 const float rstd = 1.f / sqrtf(wave_sum(s2) * (1.f / D) + LN_EPS);
; #pragma unroll
;                 for (int j2 = 0; j2 < 4; ++j2) { const int c8 = 8 * (lane + 64 * j2); u32x4 on, om;
; #pragma unroll
;                     for (int hf = 0; hf < 2; ++hf) { const int j = 2 * j2 + hf, c = c8 + 4 * hf; const f32x4 g = *(const LAS f32x4*)(LGI + c), bb = *(const LAS f32x4*)(LBI + c);
;                         f32x4 hh; hh.x = v[j].x * rstd * g.x + bb.x; hh.y = v[j].y * rstd * g.y + bb.y; hh.z = v[j].z * rstd * g.z + bb.z; hh.w = v[j].w * rstd * g.w + bb.w;
;                         const f32x4 s4 = *(const LAS f32x4*)(shp + c), c4 = *(const LAS f32x4*)(scp + c);
;                         const unsigned n0 = pk2(hh.x, hh.y), n1 = pk2(hh.z, hh.w), m0_ = pk2(hh.x * (1.f + c4.x) + s4.x, hh.y * (1.f + c4.y) + s4.y), m1_ = pk2(hh.z * (1.f + c4.z) + s4.z, hh.w * (1.f + c4.w) + s4.w);
;                         if (hf == 0) { on.x = n0; on.y = n1; om.x = m0_; om.y = m1_; } else { on.z = n0; on.w = n1; om.z = m0_; om.w = m1_; } }
;                     *(u32x4*)(HN + (size_t)m * D + c8) = on; *(u32x4*)(HM + (size_t)m * D + c8) = om; }
	v_add_f32_e32 v116, v116, v117
	ds_bpermute_b32 v117, v132, v116
	s_waitcnt lgkmcnt(0)
	v_add_f32_e32 v116, v116, v117
	ds_bpermute_b32 v117, v133, v116
	s_waitcnt lgkmcnt(0)
	v_add_f32_e32 v116, v116, v117
	ds_bpermute_b32 v117, v135, v116
	s_waitcnt lgkmcnt(0)
	v_add_f32_e32 v116, v116, v117
	ds_bpermute_b32 v117, v136, v116
	s_waitcnt lgkmcnt(0)
	v_add_f32_e32 v116, v116, v117
	ds_bpermute_b32 v117, v137, v116
	s_waitcnt lgkmcnt(0)
	v_add_f32_e32 v116, v116, v117
	v_fmamk_f32 v116, v116, 0x3a000000, v142
	v_mul_f32_e32 v117, 0x4f800000, v116
	v_cmp_gt_f32_e32 vcc, s2, v116
	s_nop 1
	v_cndmask_b32_e32 v116, v116, v117, vcc
	v_sqrt_f32_e32 v117, v116
	s_nop 0
	v_add_u32_e32 v118, -1, v117
	v_fma_f32 v119, -v118, v117, v116
	v_cmp_ge_f32_e64 s[6:7], 0, v119
	v_add_u32_e32 v119, 1, v117
	s_nop 0
	v_cndmask_b32_e64 v118, v117, v118, s[6:7]
	v_fma_f32 v117, -v119, v117, v116
	v_cmp_lt_f32_e64 s[6:7], 0, v117
	s_nop 1
	v_cndmask_b32_e64 v117, v118, v119, s[6:7]
	v_mul_f32_e32 v118, 0x37800000, v117
	v_cndmask_b32_e32 v117, v117, v118, vcc
	v_cmp_class_f32_e32 vcc, v116, v143
	s_nop 1
	v_cndmask_b32_e32 v116, v117, v116, vcc
	v_div_scale_f32 v117, s[6:7], v116, v116, 1.0
	v_rcp_f32_e32 v118, v117
	s_nop 0
	v_fma_f32 v119, -v117, v118, 1.0
	v_fmac_f32_e32 v118, v119, v118
	v_div_scale_f32 v119, vcc, 1.0, v116, 1.0
	v_mul_f32_e32 v124, v119, v118
	v_fma_f32 v125, -v117, v124, v119
	v_fmac_f32_e32 v124, v125, v118
	v_fma_f32 v117, -v117, v124, v119
	v_div_fmas_f32 v117, v117, v118, v124
	v_div_fixup_f32 v162, v117, v116, 1.0
	ds_read_b128 v[116:119], v163 offset:16384
	ds_read_b128 v[144:147], v163 offset:16400
	ds_read_b128 v[148:151], v164 offset:57344
	ds_read_b128 v[152:155], v164 offset:57360
	v_pk_mul_f32 v[124:125], v[162:163], v[126:127] op_sel_hi:[0,1]
	v_pk_fma_f32 v[126:127], v[2:3], v[124:125], v[10:11]
	v_pk_mul_f32 v[120:121], v[162:163], v[120:121] op_sel_hi:[0,1]
	s_waitcnt lgkmcnt(1)
	v_pk_add_f32 v[148:149], v[148:149], 1.0 op_sel_hi:[1,0]
	v_cvt_pk_bf16_f32 v124, v126, v127
	v_pk_fma_f32 v[116:117], v[126:127], v[148:149], v[116:117]
	v_pk_mul_f32 v[126:127], v[162:163], v[128:129] op_sel_hi:[0,1]
	v_pk_fma_f32 v[126:127], v[4:5], v[126:127], v[12:13]
	v_pk_add_f32 v[128:129], v[150:151], 1.0 op_sel_hi:[1,0]
	v_cvt_pk_bf16_f32 v116, v116, v117
	v_pk_fma_f32 v[118:119], v[126:127], v[128:129], v[118:119]
	v_cvt_pk_bf16_f32 v125, v126, v127
	v_cvt_pk_bf16_f32 v117, v118, v119
	v_pk_mul_f32 v[118:119], v[162:163], v[122:123] op_sel_hi:[0,1]
	v_pk_fma_f32 v[118:119], v[6:7], v[118:119], v[14:15]
	s_waitcnt lgkmcnt(0)
	v_pk_add_f32 v[122:123], v[152:153], 1.0 op_sel_hi:[1,0]
	v_cvt_pk_bf16_f32 v126, v118, v119
	v_pk_fma_f32 v[118:119], v[118:119], v[122:123], v[144:145]
	v_pk_mul_f32 v[122:123], v[162:163], v[156:157] op_sel_hi:[0,1]
	v_pk_fma_f32 v[122:123], v[8:9], v[122:123], v[16:17]
	v_pk_add_f32 v[128:129], v[154:155], 1.0 op_sel_hi:[1,0]
	v_cvt_pk_bf16_f32 v127, v122, v123
	v_pk_fma_f32 v[122:123], v[122:123], v[128:129], v[146:147]
	v_cvt_pk_bf16_f32 v118, v118, v119
	v_cvt_pk_bf16_f32 v119, v122, v123
	v_lshl_add_u64 v[122:123], s[4:5], 0, v[130:131]
	v_add_co_u32_e32 v152, vcc, s3, v122
	v_pk_fma_f32 v[120:121], v[20:21], v[120:121], v[28:29]
	s_nop 0
	v_addc_co_u32_e32 v153, vcc, 0, v123, vcc
	v_add_co_u32_e32 v154, vcc, s22, v122
	global_store_dwordx4 v[152:153], v[124:127], off
	s_nop 0
	v_addc_co_u32_e32 v155, vcc, 0, v123, vcc
	global_store_dwordx4 v[154:155], v[116:119], off
	ds_read_b128 v[116:119], v163 offset:18432
	ds_read_b128 v[122:125], v164 offset:59392
	ds_read_b128 v[144:147], v164 offset:59408
	ds_read_b128 v[148:151], v163 offset:18448
	v_pk_mul_f32 v[126:127], v[162:163], v[158:159] op_sel_hi:[0,1]
	v_pk_fma_f32 v[128:129], v[18:19], v[126:127], v[26:27]
	s_waitcnt lgkmcnt(2)
	v_pk_add_f32 v[122:123], v[122:123], 1.0 op_sel_hi:[1,0]
	v_pk_mul_f32 v[114:115], v[162:163], v[114:115] op_sel_hi:[0,1]
	v_pk_fma_f32 v[116:117], v[128:129], v[122:123], v[116:117]
	v_pk_add_f32 v[122:123], v[124:125], 1.0 op_sel_hi:[1,0]
	v_cvt_pk_bf16_f32 v116, v116, v117
	v_pk_fma_f32 v[118:119], v[120:121], v[122:123], v[118:119]
	v_pk_fma_f32 v[114:115], v[22:23], v[114:115], v[30:31]
	v_cvt_pk_bf16_f32 v117, v118, v119
	s_waitcnt lgkmcnt(1)
; #define LAS __attribute__((address_space(3)))
; __device__ __forceinline__ unsigned pk2(float lo, float hi) { const f32v2 v = {lo, hi}; return __builtin_bit_cast(unsigned, __builtin_convertvector(v, bf16v2)); }
; __global__ void __launch_bounds__(NTHREADS, 2) fwd(Args args) {
;     ...
; #pragma unroll
;                 for (int j2 = 0; j2 < 4; ++j2) { const int c8 = 8 * (lane + 64 * j2); u32x4 on, om;
; #pragma unroll
;                     for (int hf = 0; hf < 2; ++hf) { const int j = 2 * j2 + hf, c = c8 + 4 * hf; const f32x4 g = *(const LAS f32x4*)(LGI + c), bb = *(const LAS f32x4*)(LBI + c);
;                         f32x4 hh; hh.x = v[j].x * rstd * g.x + bb.x; hh.y = v[j].y * rstd * g.y + bb.y; hh.z = v[j].z * rstd * g.z + bb.z; hh.w = v[j].w * rstd * g.w + bb.w;
;                         const f32x4 s4 = *(const LAS f32x4*)(shp + c), c4 = *(const LAS f32x4*)(scp + c);
;                         const unsigned n0 = pk2(hh.x, hh.y), n1 = pk2(hh.z, hh.w), m0_ = pk2(hh.x * (1.f + c4.x) + s4.x, hh.y * (1.f + c4.y) + s4.y), m1_ = pk2(hh.z * (1.f + c4.z) + s4.z, hh.w * (1.f + c4.w) + s4.w);
;                         if (hf == 0) { on.x = n0; on.y = n1; om.x = m0_; om.y = m1_; } else { on.z = n0; on.w = n1; om.z = m0_; om.w = m1_; } }
;                     *(u32x4*)(HN + (size_t)m * D + c8) = on; *(u32x4*)(HM + (size_t)m * D + c8) = om; }
;             }
	v_pk_add_f32 v[118:119], v[144:145], 1.0 op_sel_hi:[1,0]
	v_cvt_pk_bf16_f32 v126, v128, v129
	v_cvt_pk_bf16_f32 v128, v114, v115
	s_waitcnt lgkmcnt(0)
	v_pk_fma_f32 v[114:115], v[114:115], v[118:119], v[148:149]
	v_cvt_pk_bf16_f32 v127, v120, v121
	v_cvt_pk_bf16_f32 v118, v114, v115
	v_pk_mul_f32 v[114:115], v[162:163], v[160:161] op_sel_hi:[0,1]
	v_pk_fma_f32 v[114:115], v[24:25], v[114:115], v[32:33]
	v_pk_add_f32 v[120:121], v[146:147], 1.0 op_sel_hi:[1,0]
	v_cvt_pk_bf16_f32 v129, v114, v115
	v_pk_fma_f32 v[114:115], v[114:115], v[120:121], v[150:151]
	v_pk_mul_f32 v[110:111], v[162:163], v[110:111] op_sel_hi:[0,1]
	v_cvt_pk_bf16_f32 v119, v114, v115
	global_store_dwordx4 v[152:153], v[126:129], off offset:1024
	global_store_dwordx4 v[154:155], v[116:119], off offset:1024
	ds_read_b128 v[114:117], v163 offset:20480
	ds_read_b128 v[118:121], v164 offset:61440
	ds_read_b128 v[122:125], v164 offset:61456
	ds_read_b128 v[126:129], v163 offset:20496
	v_pk_fma_f32 v[144:145], v[34:35], v[110:111], v[42:43]
	v_pk_mul_f32 v[112:113], v[162:163], v[112:113] op_sel_hi:[0,1]
	s_waitcnt lgkmcnt(2)
	v_pk_add_f32 v[118:119], v[118:119], 1.0 op_sel_hi:[1,0]
	v_pk_fma_f32 v[112:113], v[36:37], v[112:113], v[44:45]
	v_pk_fma_f32 v[114:115], v[144:145], v[118:119], v[114:115]
	v_pk_add_f32 v[118:119], v[120:121], 1.0 op_sel_hi:[1,0]
	v_pk_mul_f32 v[106:107], v[162:163], v[106:107] op_sel_hi:[0,1]
	v_cvt_pk_bf16_f32 v111, v112, v113
	v_pk_fma_f32 v[112:113], v[112:113], v[118:119], v[116:117]
	v_pk_fma_f32 v[106:107], v[38:39], v[106:107], v[46:47]
	s_waitcnt lgkmcnt(1)
	v_pk_add_f32 v[116:117], v[122:123], 1.0 op_sel_hi:[1,0]
	v_cvt_pk_bf16_f32 v114, v114, v115
	v_cvt_pk_bf16_f32 v115, v112, v113
	v_cvt_pk_bf16_f32 v112, v106, v107
	s_waitcnt lgkmcnt(0)
	v_pk_fma_f32 v[106:107], v[106:107], v[116:117], v[126:127]
	v_cvt_pk_bf16_f32 v110, v144, v145
	v_cvt_pk_bf16_f32 v116, v106, v107
	v_pk_mul_f32 v[106:107], v[162:163], v[108:109] op_sel_hi:[0,1]
	v_pk_fma_f32 v[106:107], v[40:41], v[106:107], v[48:49]
	v_pk_add_f32 v[108:109], v[124:125], 1.0 op_sel_hi:[1,0]
	v_cvt_pk_bf16_f32 v113, v106, v107
	v_pk_fma_f32 v[106:107], v[106:107], v[108:109], v[128:129]
	v_pk_mul_f32 v[102:103], v[162:163], v[102:103] op_sel_hi:[0,1]
	v_cvt_pk_bf16_f32 v117, v106, v107
	global_store_dwordx4 v[152:153], v[110:113], off offset:2048
	global_store_dwordx4 v[154:155], v[114:117], off offset:2048
	ds_read_b128 v[106:109], v163 offset:22528
	ds_read_b128 v[110:113], v163 offset:22544
	ds_read_b128 v[114:117], v164 offset:63488
	ds_read_b128 v[118:121], v164 offset:63504
	v_pk_fma_f32 v[122:123], v[50:51], v[102:103], v[58:59]
	v_pk_mul_f32 v[104:105], v[162:163], v[104:105] op_sel_hi:[0,1]
	v_pk_fma_f32 v[104:105], v[52:53], v[104:105], v[60:61]
	s_waitcnt lgkmcnt(1)
	v_pk_add_f32 v[114:115], v[114:115], 1.0 op_sel_hi:[1,0]
	v_pk_mul_f32 v[98:99], v[162:163], v[98:99] op_sel_hi:[0,1]
	v_pk_fma_f32 v[106:107], v[122:123], v[114:115], v[106:107]
	v_pk_add_f32 v[114:115], v[116:117], 1.0 op_sel_hi:[1,0]
	v_cvt_pk_bf16_f32 v103, v104, v105
	v_pk_fma_f32 v[104:105], v[104:105], v[114:115], v[108:109]
	v_pk_fma_f32 v[98:99], v[54:55], v[98:99], v[62:63]
	s_waitcnt lgkmcnt(0)
	v_pk_add_f32 v[108:109], v[118:119], 1.0 op_sel_hi:[1,0]
	v_cvt_pk_bf16_f32 v106, v106, v107
	v_cvt_pk_bf16_f32 v107, v104, v105
	v_cvt_pk_bf16_f32 v104, v98, v99
	v_pk_fma_f32 v[98:99], v[98:99], v[108:109], v[110:111]
	v_cvt_pk_bf16_f32 v102, v122, v123
	v_cvt_pk_bf16_f32 v108, v98, v99
	v_pk_mul_f32 v[98:99], v[162:163], v[100:101] op_sel_hi:[0,1]
	v_pk_fma_f32 v[98:99], v[56:57], v[98:99], v[64:65]
	v_pk_add_f32 v[100:101], v[120:121], 1.0 op_sel_hi:[1,0]
	v_cvt_pk_bf16_f32 v105, v98, v99
	v_pk_fma_f32 v[98:99], v[98:99], v[100:101], v[112:113]
	s_andn2_b64 vcc, exec, s[18:19]
	v_cvt_pk_bf16_f32 v109, v98, v99
	global_store_dwordx4 v[152:153], v[102:105], off offset:3072
	global_store_dwordx4 v[154:155], v[106:109], off offset:3072
	s_cbranch_vccnz .LBB0_113
	s_cmpk_lt_i32 s24, 0x4000
	s_movk_i32 s18, 0x2000
	s_cselect_b64 s[6:7], -1, 0
	s_cmpk_gt_i32 s24, 0x3fff
	s_movk_i32 s19, 0x2000
	s_cbranch_scc1 .LBB0_121
	s_ashr_i32 s19, s24, 31
	s_lshr_b32 s19, s19, 20
	s_add_i32 s19, s24, s19
	s_ashr_i32 s19, s19, 12
	s_lshl_b32 s19, s19, 11
